# speedup vs baseline: 1.0128x; 1.0067x over previous
.LBB1_18:
	s_and_saveexec_b64 s[44:45], s[8:9]
	global_load_dwordx4 v[84:87], v[102:103], off offset:-3072
	global_load_dwordx4 v[88:91], v[102:103], off offset:-2048
	global_load_dwordx4 v[92:95], v[102:103], off offset:-1024
	global_load_dwordx4 v[80:83], v[102:103], off
	s_mov_b64 exec, s[44:45]
	s_add_i32 s27, s26, 2
	s_cmp_gt_u32 s26, 17
	s_cselect_b64 s[16:17], -1, 0
	s_cmp_lt_u32 s26, 18
	s_cselect_b64 s[18:19], -1, 0
	s_and_b64 s[20:21], s[18:19], exec
	s_cselect_b32 s4, s27, s26
	s_lshl_b32 s4, s4, 11
	s_lshl_b64 s[20:21], s[4:5], 2
	v_lshl_add_u64 v[64:65], v[96:97], 0, s[20:21]
	v_lshl_add_u64 v[66:67], v[98:99], 0, s[20:21]
	s_and_saveexec_b64 s[44:45], s[18:19]
	global_load_dwordx4 v[68:71], v[64:65], off nt
	s_and_b64 exec, exec, s[0:1]
	global_load_dwordx4 v[64:67], v[66:67], off nt
	s_mov_b64 exec, s[44:45]
	s_waitcnt vmcnt(7)
	v_pk_fma_f32 v[104:105], v[76:77], v[76:77], v[104:105]
	v_pk_fma_f32 v[106:107], v[78:79], v[78:79], v[106:107]
	v_cvt_pk_f16_f32 v79, v78, v79
	v_cvt_pk_f16_f32 v78, v76, v77
	ds_write_b64 v109, v[78:79] offset:5120
	s_and_saveexec_b64 s[20:21], s[0:1]
	s_cbranch_execz .LBB1_20
	s_waitcnt vmcnt(6)
	v_pk_fma_f32 v[104:105], v[72:73], v[72:73], v[104:105]
	v_pk_fma_f32 v[106:107], v[74:75], v[74:75], v[106:107]
	v_cvt_pk_f16_f32 v75, v74, v75
	v_cvt_pk_f16_f32 v74, v72, v73
	ds_write_b64 v109, v[74:75] offset:8320

.LBB1_29:
	s_add_i32 s20, s26, 1
	s_and_b64 s[2:3], s[18:19], exec
	s_cselect_b32 s2, s27, s20
	s_lshl_b32 s4, s2, 12
	s_waitcnt vmcnt(6)
	v_lshl_add_u64 v[72:73], v[100:101], 0, s[4:5]
	s_and_saveexec_b64 s[44:45], s[8:9]
	s_and_b64 exec, exec, s[18:19]
	global_load_dwordx4 v[92:95], v[72:73], off
	global_load_dwordx4 v[80:83], v[72:73], off offset:1024
	global_load_dwordx4 v[88:91], v[72:73], off offset:2048
	global_load_dwordx4 v[84:87], v[72:73], off offset:3072
	s_mov_b64 exec, s[44:45]
	s_add_i32 s2, s26, 3
	s_cmp_lt_u32 s26, 17
	s_cselect_b32 s2, s2, s20
	s_lshl_b32 s4, s2, 11
	s_lshl_b64 s[2:3], s[4:5], 2
	v_lshl_add_u64 v[72:73], v[96:97], 0, s[2:3]
	v_lshl_add_u64 v[74:75], v[98:99], 0, s[2:3]
	s_and_saveexec_b64 s[44:45], s[18:19]
	global_load_dwordx4 v[76:79], v[72:73], off nt
	s_and_b64 exec, exec, s[0:1]
	global_load_dwordx4 v[72:75], v[74:75], off nt
	s_mov_b64 exec, s[44:45]
	v_lshl_add_u64 v[102:103], v[102:103], 0, s[14:15]
	s_and_b64 vcc, exec, s[16:17]
	s_cbranch_vccnz .LBB1_31
	s_mov_b32 s26, s27
	s_branch .LBB1_7
